# gate/up layer-0 SwiGLU epilogue: sigmoid reciprocals of two accumulator pairs from one reciprocal of their product (2 rcp + 3 pk_mul instead of 4 rcp), lower clamp -60 on the gate pre-activation via m
# baseline (speedup 1.0000x reference)
.LBB0_1546:
	s_mov_b32 s73, 0xc2700000
	v_mov_b32_e32 v184, 0x41898193
	v_lshlrev_b32_e32 v150, 16, v86
	v_and_b32_e32 v151, 0xffff0000, v86
	v_mul_f32_e32 v158, 0x3d800000, v177
	v_pk_fma_f32 v[130:131], v[158:159], v[130:131], v[150:151] op_sel_hi:[0,1,1]
	v_med3_f32 v130, v130, s73, v184
	v_med3_f32 v131, v131, s73, v184
	v_exp_f32_e64 v178, -v130
	v_exp_f32_e64 v179, -v131
	v_lshlrev_b32_e32 v156, 16, v87
	v_and_b32_e32 v157, 0xffff0000, v87
	v_lshlrev_b32_e32 v152, 16, v82
	v_pk_add_f32 v[178:179], v[178:179], 1.0 op_sel_hi:[1,0]
	v_and_b32_e32 v153, 0xffff0000, v82
	v_lshlrev_b32_e32 v154, 16, v83
	v_and_b32_e32 v155, 0xffff0000, v83
	v_pk_fma_f32 v[132:133], v[158:159], v[132:133], v[156:157] op_sel_hi:[0,1,1]
	v_pk_fma_f32 v[134:135], v[158:159], v[134:135], v[152:153] op_sel_hi:[0,1,1]
	v_pk_fma_f32 v[136:137], v[158:159], v[136:137], v[154:155] op_sel_hi:[0,1,1]
	v_med3_f32 v134, v134, s70, v167
	v_med3_f32 v135, v135, s70, v167
	v_med3_f32 v132, v132, s73, v184
	v_med3_f32 v133, v133, s73, v184
	v_pk_mul_f32 v[130:131], v[130:131], v[134:135]
	v_med3_f32 v134, v136, s70, v167
	v_med3_f32 v135, v137, s70, v167
	v_exp_f32_e64 v136, -v132
	v_exp_f32_e64 v137, -v133
	v_lshlrev_b32_e32 v86, 16, v88
	v_and_b32_e32 v87, 0xffff0000, v88
	v_pk_fma_f32 v[122:123], v[158:159], v[122:123], v[86:87] op_sel_hi:[0,1,1]
	v_pk_add_f32 v[136:137], v[136:137], 1.0 op_sel_hi:[1,0]
	v_med3_f32 v122, v122, s73, v184
	v_pk_mul_f32 v[180:181], v[178:179], v[136:137]
	v_rcp_f32_e32 v180, v180
	v_rcp_f32_e32 v181, v181
	s_nop 0
	v_pk_mul_f32 v[182:183], v[180:181], v[136:137]
	v_pk_mul_f32 v[136:137], v[180:181], v[178:179]
	v_pk_mul_f32 v[130:131], v[130:131], v[182:183]
	v_med3_f32 v123, v123, s73, v184
	v_lshlrev_b32_e32 v88, 16, v89
	v_and_b32_e32 v89, 0xffff0000, v89
	v_pk_mul_f32 v[132:133], v[132:133], v[136:137]
	v_lshlrev_b32_e32 v82, 16, v84
	v_pk_mul_f32 v[132:133], v[132:133], v[134:135]
	v_exp_f32_e64 v134, -v122
	v_exp_f32_e64 v135, -v123
	v_and_b32_e32 v83, 0xffff0000, v84
	v_lshlrev_b32_e32 v84, 16, v85
	v_and_b32_e32 v85, 0xffff0000, v85
	v_pk_add_f32 v[134:135], v[134:135], 1.0 op_sel_hi:[1,0]
	v_pk_fma_f32 v[124:125], v[158:159], v[124:125], v[88:89] op_sel_hi:[0,1,1]
	v_pk_fma_f32 v[126:127], v[158:159], v[126:127], v[82:83] op_sel_hi:[0,1,1]
	v_pk_fma_f32 v[128:129], v[158:159], v[128:129], v[84:85] op_sel_hi:[0,1,1]
	v_med3_f32 v126, v126, s70, v167
	v_med3_f32 v127, v127, s70, v167
	v_med3_f32 v124, v124, s73, v184
	v_med3_f32 v125, v125, s73, v184
	v_pk_mul_f32 v[122:123], v[122:123], v[126:127]
	v_med3_f32 v126, v128, s70, v167
	v_med3_f32 v127, v129, s70, v167
	v_exp_f32_e64 v128, -v124
	v_exp_f32_e64 v129, -v125
	v_mov_b32_e32 v142, v0
	s_and_b64 vcc, exec, s[6:7]
	v_pk_add_f32 v[128:129], v[128:129], 1.0 op_sel_hi:[1,0]
	v_readfirstlane_b32 s69, v142
	v_pk_mul_f32 v[180:181], v[134:135], v[128:129]
	v_rcp_f32_e32 v180, v180
	v_rcp_f32_e32 v181, v181
	s_nop 0
	v_pk_mul_f32 v[182:183], v[180:181], v[128:129]
	v_pk_mul_f32 v[128:129], v[180:181], v[134:135]
	v_pk_mul_f32 v[122:123], v[122:123], v[182:183]
	s_ashr_i32 s8, s69, 6
	s_mul_i32 s9, s8, 0xb00
	s_add_i32 s71, s9, 0
	v_pk_mul_f32 v[124:125], v[124:125], v[128:129]
	v_and_b32_e32 v147, 15, v142
	v_pk_mul_f32 v[124:125], v[124:125], v[126:127]
	v_mov_b32_e32 v126, 0
	v_mov_b32_e32 v127, 0
	v_cvt_pk_fp8_f32 v126, v130, v131
	v_cvt_pk_fp8_f32 v127, v122, v123
	v_lshrrev_b32_e32 v123, 1, v142
	s_add_i32 s71, s71, 0x20000
	v_cvt_pk_fp8_f32 v126, v132, v133 op_sel:[0,0,1]
	v_cvt_pk_fp8_f32 v127, v124, v125 op_sel:[0,0,1]
	v_mul_f32_e32 v124, 0x3d800000, v176
	v_mul_u32_u24_e32 v122, 48, v147
	v_and_b32_e32 v123, 24, v123
	v_pk_fma_f32 v[114:115], v[124:125], v[114:115], v[150:151] op_sel_hi:[0,1,1]
	v_add3_u32 v122, s71, v122, v123
	v_med3_f32 v114, v114, s73, v184
	v_med3_f32 v115, v115, s73, v184
	ds_write_b64 v122, v[126:127]
	v_exp_f32_e64 v126, -v114
	v_exp_f32_e64 v127, -v115
	v_pk_fma_f32 v[116:117], v[124:125], v[116:117], v[156:157] op_sel_hi:[0,1,1]
	v_pk_fma_f32 v[118:119], v[124:125], v[118:119], v[152:153] op_sel_hi:[0,1,1]
	v_pk_fma_f32 v[120:121], v[124:125], v[120:121], v[154:155] op_sel_hi:[0,1,1]
	v_pk_add_f32 v[126:127], v[126:127], 1.0 op_sel_hi:[1,0]
	v_med3_f32 v118, v118, s70, v167
	v_med3_f32 v119, v119, s70, v167
	v_med3_f32 v116, v116, s73, v184
	v_med3_f32 v117, v117, s73, v184
	v_pk_fma_f32 v[106:107], v[124:125], v[106:107], v[86:87] op_sel_hi:[0,1,1]
	v_pk_mul_f32 v[114:115], v[114:115], v[118:119]
	v_med3_f32 v118, v120, s70, v167
	v_med3_f32 v119, v121, s70, v167
	v_exp_f32_e64 v120, -v116
	v_exp_f32_e64 v121, -v117
	v_med3_f32 v106, v106, s73, v184
	v_med3_f32 v107, v107, s73, v184
	v_pk_fma_f32 v[108:109], v[124:125], v[108:109], v[88:89] op_sel_hi:[0,1,1]
	v_pk_add_f32 v[120:121], v[120:121], 1.0 op_sel_hi:[1,0]
	v_pk_fma_f32 v[110:111], v[124:125], v[110:111], v[82:83] op_sel_hi:[0,1,1]
	v_pk_mul_f32 v[180:181], v[126:127], v[120:121]
	v_rcp_f32_e32 v180, v180
	v_rcp_f32_e32 v181, v181
	s_nop 0
	v_pk_mul_f32 v[182:183], v[180:181], v[120:121]
	v_pk_mul_f32 v[120:121], v[180:181], v[126:127]
	v_pk_mul_f32 v[114:115], v[114:115], v[182:183]
	v_pk_fma_f32 v[112:113], v[124:125], v[112:113], v[84:85] op_sel_hi:[0,1,1]
	v_med3_f32 v110, v110, s70, v167
	v_med3_f32 v111, v111, s70, v167
	v_pk_mul_f32 v[116:117], v[116:117], v[120:121]
	v_med3_f32 v108, v108, s73, v184
	v_pk_mul_f32 v[116:117], v[116:117], v[118:119]
	v_exp_f32_e64 v118, -v106
	v_exp_f32_e64 v119, -v107
	v_med3_f32 v109, v109, s73, v184
	s_ashr_i32 s69, s69, 2
	s_andn2_b32 s69, s69, 63
	v_pk_add_f32 v[118:119], v[118:119], 1.0 op_sel_hi:[1,0]
	s_lshl_b32 s8, s8, 5
	s_lshl_b32 s9, s80, 7
	s_and_b32 s8, s8, 0x60
	s_or_b32 s8, s8, s9
	s_ashr_i32 s9, s8, 31
	v_pk_mul_f32 v[106:107], v[106:107], v[110:111]
	v_med3_f32 v110, v112, s70, v167
	v_med3_f32 v111, v113, s70, v167
	v_exp_f32_e64 v112, -v108
	v_exp_f32_e64 v113, -v109
	s_nop 0
	v_pk_add_f32 v[112:113], v[112:113], 1.0 op_sel_hi:[1,0]
	s_nop 0
	v_pk_mul_f32 v[180:181], v[118:119], v[112:113]
	v_rcp_f32_e32 v180, v180
	v_rcp_f32_e32 v181, v181
	s_nop 0
	v_pk_mul_f32 v[182:183], v[180:181], v[112:113]
	v_pk_mul_f32 v[112:113], v[180:181], v[118:119]
	v_pk_mul_f32 v[106:107], v[106:107], v[182:183]
	s_nop 0
	v_pk_mul_f32 v[108:109], v[108:109], v[112:113]
	s_nop 0
	v_pk_mul_f32 v[108:109], v[108:109], v[110:111]
	v_mov_b32_e32 v110, 0
	v_mov_b32_e32 v111, 0
	v_cvt_pk_fp8_f32 v110, v114, v115
	v_cvt_pk_fp8_f32 v111, v106, v107
	v_bfe_u32 v106, v142, 1, 5
	v_mul_u32_u24_e32 v107, 48, v106
	v_cvt_pk_fp8_f32 v110, v116, v117 op_sel:[0,0,1]
	v_cvt_pk_fp8_f32 v111, v108, v109 op_sel:[0,0,1]
	v_lshlrev_b32_e32 v108, 4, v142
	v_and_b32_e32 v142, 16, v108
	v_lshl_or_b32 v106, s78, 8, v106
	ds_write_b64 v122, v[110:111] offset:768
	v_add3_u32 v108, s71, v107, v142
	v_add_u32_e32 v106, s69, v106
	ds_read_b128 v[110:113], v108
	v_ashrrev_i32_e32 v107, 31, v106
	v_lshlrev_b64 v[114:115], 10, v[106:107]
	v_lshl_add_u64 v[114:115], s[16:17], 0, v[114:115]
	v_lshl_add_u64 v[114:115], v[114:115], 0, s[8:9]
	v_lshl_add_u64 v[114:115], v[114:115], 0, v[142:143]
	s_waitcnt lgkmcnt(0)
	global_store_dwordx4 v[114:115], v[110:113], off
	s_nop 1
	v_mul_f32_e32 v110, 0x3d800000, v175
	v_pk_fma_f32 v[98:99], v[110:111], v[98:99], v[150:151] op_sel_hi:[0,1,1]
	v_med3_f32 v98, v98, s73, v184
	v_med3_f32 v99, v99, s73, v184
	v_exp_f32_e64 v112, -v98
	v_exp_f32_e64 v113, -v99
	v_pk_fma_f32 v[100:101], v[110:111], v[100:101], v[156:157] op_sel_hi:[0,1,1]
	v_pk_fma_f32 v[102:103], v[110:111], v[102:103], v[152:153] op_sel_hi:[0,1,1]
	v_pk_fma_f32 v[104:105], v[110:111], v[104:105], v[154:155] op_sel_hi:[0,1,1]
	v_pk_add_f32 v[112:113], v[112:113], 1.0 op_sel_hi:[1,0]
	v_med3_f32 v102, v102, s70, v167
	v_med3_f32 v103, v103, s70, v167
	v_med3_f32 v100, v100, s73, v184
	v_med3_f32 v101, v101, s73, v184
	v_pk_fma_f32 v[90:91], v[110:111], v[90:91], v[86:87] op_sel_hi:[0,1,1]
	v_pk_mul_f32 v[98:99], v[98:99], v[102:103]
	v_med3_f32 v102, v104, s70, v167
	v_med3_f32 v103, v105, s70, v167
	v_exp_f32_e64 v104, -v100
	v_exp_f32_e64 v105, -v101
	v_med3_f32 v90, v90, s73, v184
	v_med3_f32 v91, v91, s73, v184
	v_pk_fma_f32 v[92:93], v[110:111], v[92:93], v[88:89] op_sel_hi:[0,1,1]
	v_pk_add_f32 v[104:105], v[104:105], 1.0 op_sel_hi:[1,0]
	v_pk_fma_f32 v[94:95], v[110:111], v[94:95], v[82:83] op_sel_hi:[0,1,1]
	v_pk_mul_f32 v[180:181], v[112:113], v[104:105]
	v_rcp_f32_e32 v180, v180
	v_rcp_f32_e32 v181, v181
	s_nop 0
	v_pk_mul_f32 v[182:183], v[180:181], v[104:105]
	v_pk_mul_f32 v[104:105], v[180:181], v[112:113]
	v_pk_mul_f32 v[98:99], v[98:99], v[182:183]
	v_pk_fma_f32 v[96:97], v[110:111], v[96:97], v[84:85] op_sel_hi:[0,1,1]
	v_med3_f32 v94, v94, s70, v167
	v_med3_f32 v95, v95, s70, v167
	v_pk_mul_f32 v[100:101], v[100:101], v[104:105]
	v_med3_f32 v92, v92, s73, v184
	v_pk_mul_f32 v[100:101], v[100:101], v[102:103]
	v_exp_f32_e64 v102, -v90
	v_exp_f32_e64 v103, -v91
	v_med3_f32 v93, v93, s73, v184
	v_pk_add_f32 v[102:103], v[102:103], 1.0 op_sel_hi:[1,0]
	s_nop 0
	s_nop 0
	s_nop 0
	v_pk_mul_f32 v[90:91], v[90:91], v[94:95]
	v_med3_f32 v94, v96, s70, v167
	v_med3_f32 v95, v97, s70, v167
	v_exp_f32_e64 v96, -v92
	v_exp_f32_e64 v97, -v93
	s_nop 0
	v_pk_add_f32 v[96:97], v[96:97], 1.0 op_sel_hi:[1,0]
	s_nop 0
	v_pk_mul_f32 v[180:181], v[102:103], v[96:97]
	v_rcp_f32_e32 v180, v180
	v_rcp_f32_e32 v181, v181
	s_nop 0
	v_pk_mul_f32 v[182:183], v[180:181], v[96:97]
	v_pk_mul_f32 v[96:97], v[180:181], v[102:103]
	v_pk_mul_f32 v[90:91], v[90:91], v[182:183]
	s_nop 0
	v_pk_mul_f32 v[92:93], v[92:93], v[96:97]
	s_nop 0
	v_pk_mul_f32 v[92:93], v[92:93], v[94:95]
	v_mov_b32_e32 v95, v143
	v_cvt_pk_fp8_f32 v95, v90, v91
	v_mul_f32_e32 v90, 0x3d800000, v174
	v_pk_fma_f32 v[74:75], v[90:91], v[74:75], v[150:151] op_sel_hi:[0,1,1]
	v_med3_f32 v74, v74, s73, v184
	v_med3_f32 v75, v75, s73, v184
	v_cvt_pk_fp8_f32 v95, v92, v93 op_sel:[0,0,1]
	v_exp_f32_e64 v92, -v74
	v_exp_f32_e64 v93, -v75
	v_pk_fma_f32 v[76:77], v[90:91], v[76:77], v[156:157] op_sel_hi:[0,1,1]
	v_pk_fma_f32 v[78:79], v[90:91], v[78:79], v[152:153] op_sel_hi:[0,1,1]
	v_pk_fma_f32 v[80:81], v[90:91], v[80:81], v[154:155] op_sel_hi:[0,1,1]
	v_pk_add_f32 v[92:93], v[92:93], 1.0 op_sel_hi:[1,0]
	v_med3_f32 v78, v78, s70, v167
	v_med3_f32 v79, v79, s70, v167
	v_med3_f32 v76, v76, s73, v184
	v_med3_f32 v77, v77, s73, v184
	v_pk_fma_f32 v[66:67], v[90:91], v[66:67], v[86:87] op_sel_hi:[0,1,1]
	v_pk_mul_f32 v[74:75], v[74:75], v[78:79]
	v_med3_f32 v78, v80, s70, v167
	v_med3_f32 v79, v81, s70, v167
	v_exp_f32_e64 v80, -v76
	v_exp_f32_e64 v81, -v77
	v_med3_f32 v66, v66, s73, v184
	v_med3_f32 v67, v67, s73, v184
	v_pk_fma_f32 v[68:69], v[90:91], v[68:69], v[88:89] op_sel_hi:[0,1,1]
	v_pk_add_f32 v[80:81], v[80:81], 1.0 op_sel_hi:[1,0]
	v_pk_fma_f32 v[70:71], v[90:91], v[70:71], v[82:83] op_sel_hi:[0,1,1]
	v_pk_mul_f32 v[180:181], v[92:93], v[80:81]
	v_rcp_f32_e32 v180, v180
	v_rcp_f32_e32 v181, v181
	s_nop 0
	v_pk_mul_f32 v[182:183], v[180:181], v[80:81]
	v_pk_mul_f32 v[80:81], v[180:181], v[92:93]
	v_pk_mul_f32 v[74:75], v[74:75], v[182:183]
	v_pk_fma_f32 v[72:73], v[90:91], v[72:73], v[84:85] op_sel_hi:[0,1,1]
	v_med3_f32 v70, v70, s70, v167
	v_med3_f32 v71, v71, s70, v167
	v_pk_mul_f32 v[76:77], v[76:77], v[80:81]
	v_med3_f32 v68, v68, s73, v184
	v_pk_mul_f32 v[76:77], v[76:77], v[78:79]
	v_exp_f32_e64 v78, -v66
	v_exp_f32_e64 v79, -v67
	v_med3_f32 v69, v69, s73, v184
	v_mov_b32_e32 v94, v143
	v_cvt_pk_fp8_f32 v94, v98, v99
	v_pk_add_f32 v[78:79], v[78:79], 1.0 op_sel_hi:[1,0]
	v_cvt_pk_fp8_f32 v94, v100, v101 op_sel:[0,0,1]
	ds_write_b64 v122, v[94:95]
	s_nop 0
	v_pk_mul_f32 v[66:67], v[66:67], v[70:71]
	v_med3_f32 v70, v72, s70, v167
	v_med3_f32 v71, v73, s70, v167
	v_exp_f32_e64 v72, -v68
	v_exp_f32_e64 v73, -v69
	s_nop 0
	v_pk_add_f32 v[72:73], v[72:73], 1.0 op_sel_hi:[1,0]
	s_nop 0
	v_pk_mul_f32 v[180:181], v[78:79], v[72:73]
	v_rcp_f32_e32 v180, v180
	v_rcp_f32_e32 v181, v181
	s_nop 0
	v_pk_mul_f32 v[182:183], v[180:181], v[72:73]
	v_pk_mul_f32 v[72:73], v[180:181], v[78:79]
	v_pk_mul_f32 v[66:67], v[66:67], v[182:183]
	s_nop 0
	v_pk_mul_f32 v[68:69], v[68:69], v[72:73]
	s_nop 0
	v_pk_mul_f32 v[68:69], v[68:69], v[70:71]
	v_mov_b32_e32 v70, v143
	v_mov_b32_e32 v71, v143
	v_cvt_pk_fp8_f32 v70, v74, v75
	v_cvt_pk_fp8_f32 v71, v66, v67
	v_cvt_pk_fp8_f32 v70, v76, v77 op_sel:[0,0,1]
	v_cvt_pk_fp8_f32 v71, v68, v69 op_sel:[0,0,1]
	ds_write_b64 v122, v[70:71] offset:768
	v_or_b32_e32 v70, 32, v106
	ds_read_b128 v[66:69], v108
	v_ashrrev_i32_e32 v71, 31, v70
	v_lshlrev_b64 v[70:71], 10, v[70:71]
	v_lshl_add_u64 v[70:71], s[16:17], 0, v[70:71]
	v_lshl_add_u64 v[70:71], v[70:71], 0, s[8:9]
	v_lshl_add_u64 v[70:71], v[70:71], 0, v[142:143]
	s_waitcnt lgkmcnt(0)
	global_store_dwordx4 v[70:71], v[66:69], off
	s_nop 1
	v_mul_f32_e32 v66, 0x3d800000, v173
	v_pk_fma_f32 v[58:59], v[66:67], v[58:59], v[150:151] op_sel_hi:[0,1,1]
	v_med3_f32 v58, v58, s73, v184
	v_med3_f32 v59, v59, s73, v184
	v_exp_f32_e64 v68, -v58
	v_exp_f32_e64 v69, -v59
	v_pk_fma_f32 v[60:61], v[66:67], v[60:61], v[156:157] op_sel_hi:[0,1,1]
	v_pk_fma_f32 v[62:63], v[66:67], v[62:63], v[152:153] op_sel_hi:[0,1,1]
	v_pk_fma_f32 v[64:65], v[66:67], v[64:65], v[154:155] op_sel_hi:[0,1,1]
	v_pk_add_f32 v[68:69], v[68:69], 1.0 op_sel_hi:[1,0]
	v_med3_f32 v62, v62, s70, v167
	v_med3_f32 v63, v63, s70, v167
	v_med3_f32 v60, v60, s73, v184
	v_med3_f32 v61, v61, s73, v184
	v_pk_fma_f32 v[50:51], v[66:67], v[50:51], v[86:87] op_sel_hi:[0,1,1]
	v_pk_mul_f32 v[58:59], v[58:59], v[62:63]
	v_med3_f32 v62, v64, s70, v167
	v_med3_f32 v63, v65, s70, v167
	v_exp_f32_e64 v64, -v60
	v_exp_f32_e64 v65, -v61
	v_med3_f32 v50, v50, s73, v184
	v_med3_f32 v51, v51, s73, v184
	v_pk_fma_f32 v[52:53], v[66:67], v[52:53], v[88:89] op_sel_hi:[0,1,1]
	v_pk_add_f32 v[64:65], v[64:65], 1.0 op_sel_hi:[1,0]
	v_pk_fma_f32 v[54:55], v[66:67], v[54:55], v[82:83] op_sel_hi:[0,1,1]
	v_pk_mul_f32 v[180:181], v[68:69], v[64:65]
	v_rcp_f32_e32 v180, v180
	v_rcp_f32_e32 v181, v181
	s_nop 0
	v_pk_mul_f32 v[182:183], v[180:181], v[64:65]
	v_pk_mul_f32 v[64:65], v[180:181], v[68:69]
	v_pk_mul_f32 v[58:59], v[58:59], v[182:183]
	v_pk_fma_f32 v[56:57], v[66:67], v[56:57], v[84:85] op_sel_hi:[0,1,1]
	v_med3_f32 v54, v54, s70, v167
	v_med3_f32 v55, v55, s70, v167
	v_pk_mul_f32 v[60:61], v[60:61], v[64:65]
	v_med3_f32 v52, v52, s73, v184
	v_pk_mul_f32 v[60:61], v[60:61], v[62:63]
	v_exp_f32_e64 v62, -v50
	v_exp_f32_e64 v63, -v51
	v_med3_f32 v53, v53, s73, v184
	v_pk_add_f32 v[62:63], v[62:63], 1.0 op_sel_hi:[1,0]
	s_nop 0
	s_nop 0
	s_nop 0
	v_pk_mul_f32 v[50:51], v[50:51], v[54:55]
	v_med3_f32 v54, v56, s70, v167
	v_med3_f32 v55, v57, s70, v167
	v_exp_f32_e64 v56, -v52
	v_exp_f32_e64 v57, -v53
	s_nop 0
	v_pk_add_f32 v[56:57], v[56:57], 1.0 op_sel_hi:[1,0]
	s_nop 0
	v_pk_mul_f32 v[180:181], v[62:63], v[56:57]
	v_rcp_f32_e32 v180, v180
	v_rcp_f32_e32 v181, v181
	s_nop 0
	v_pk_mul_f32 v[182:183], v[180:181], v[56:57]
	v_pk_mul_f32 v[56:57], v[180:181], v[62:63]
	v_pk_mul_f32 v[50:51], v[50:51], v[182:183]
	s_nop 0
	v_pk_mul_f32 v[52:53], v[52:53], v[56:57]
	s_nop 0
	v_pk_mul_f32 v[52:53], v[52:53], v[54:55]
	v_mov_b32_e32 v55, v143
	v_cvt_pk_fp8_f32 v55, v50, v51
	v_mul_f32_e32 v50, 0x3d800000, v172
	v_pk_fma_f32 v[42:43], v[50:51], v[42:43], v[150:151] op_sel_hi:[0,1,1]
	v_med3_f32 v42, v42, s73, v184
	v_med3_f32 v43, v43, s73, v184
	v_cvt_pk_fp8_f32 v55, v52, v53 op_sel:[0,0,1]
	v_exp_f32_e64 v52, -v42
	v_exp_f32_e64 v53, -v43
	v_pk_fma_f32 v[44:45], v[50:51], v[44:45], v[156:157] op_sel_hi:[0,1,1]
	v_pk_fma_f32 v[46:47], v[50:51], v[46:47], v[152:153] op_sel_hi:[0,1,1]
	v_pk_fma_f32 v[48:49], v[50:51], v[48:49], v[154:155] op_sel_hi:[0,1,1]
	v_pk_add_f32 v[52:53], v[52:53], 1.0 op_sel_hi:[1,0]
	v_med3_f32 v46, v46, s70, v167
	v_med3_f32 v47, v47, s70, v167
	v_med3_f32 v44, v44, s73, v184
	v_med3_f32 v45, v45, s73, v184
	v_pk_fma_f32 v[34:35], v[50:51], v[34:35], v[86:87] op_sel_hi:[0,1,1]
	v_pk_mul_f32 v[42:43], v[42:43], v[46:47]
	v_med3_f32 v46, v48, s70, v167
	v_med3_f32 v47, v49, s70, v167
	v_exp_f32_e64 v48, -v44
	v_exp_f32_e64 v49, -v45
	v_med3_f32 v34, v34, s73, v184
	v_med3_f32 v35, v35, s73, v184
	v_pk_fma_f32 v[36:37], v[50:51], v[36:37], v[88:89] op_sel_hi:[0,1,1]
	v_pk_add_f32 v[48:49], v[48:49], 1.0 op_sel_hi:[1,0]
	v_pk_fma_f32 v[38:39], v[50:51], v[38:39], v[82:83] op_sel_hi:[0,1,1]
	v_pk_mul_f32 v[180:181], v[52:53], v[48:49]
	v_rcp_f32_e32 v180, v180
	v_rcp_f32_e32 v181, v181
	s_nop 0
	v_pk_mul_f32 v[182:183], v[180:181], v[48:49]
	v_pk_mul_f32 v[48:49], v[180:181], v[52:53]
	v_pk_mul_f32 v[42:43], v[42:43], v[182:183]
	v_pk_fma_f32 v[40:41], v[50:51], v[40:41], v[84:85] op_sel_hi:[0,1,1]
	v_med3_f32 v38, v38, s70, v167
	v_med3_f32 v39, v39, s70, v167
	v_pk_mul_f32 v[44:45], v[44:45], v[48:49]
	v_med3_f32 v36, v36, s73, v184
	v_pk_mul_f32 v[44:45], v[44:45], v[46:47]
	v_exp_f32_e64 v46, -v34
	v_exp_f32_e64 v47, -v35
	v_med3_f32 v37, v37, s73, v184
	v_mov_b32_e32 v54, v143
	v_cvt_pk_fp8_f32 v54, v58, v59
	v_pk_add_f32 v[46:47], v[46:47], 1.0 op_sel_hi:[1,0]
	v_cvt_pk_fp8_f32 v54, v60, v61 op_sel:[0,0,1]
	ds_write_b64 v122, v[54:55]
	s_nop 0
	v_pk_mul_f32 v[34:35], v[34:35], v[38:39]
	v_med3_f32 v38, v40, s70, v167
	v_med3_f32 v39, v41, s70, v167
	v_exp_f32_e64 v40, -v36
	v_exp_f32_e64 v41, -v37
	s_nop 0
	v_pk_add_f32 v[40:41], v[40:41], 1.0 op_sel_hi:[1,0]
	s_nop 0
	v_pk_mul_f32 v[180:181], v[46:47], v[40:41]
	v_rcp_f32_e32 v180, v180
	v_rcp_f32_e32 v181, v181
	s_nop 0
	v_pk_mul_f32 v[182:183], v[180:181], v[40:41]
	v_pk_mul_f32 v[40:41], v[180:181], v[46:47]
	v_pk_mul_f32 v[34:35], v[34:35], v[182:183]
	s_nop 0
	v_pk_mul_f32 v[36:37], v[36:37], v[40:41]
	s_nop 0
	v_pk_mul_f32 v[36:37], v[36:37], v[38:39]
	v_mov_b32_e32 v38, v143
	v_mov_b32_e32 v39, v143
	v_cvt_pk_fp8_f32 v38, v42, v43
	v_cvt_pk_fp8_f32 v39, v34, v35
	v_cvt_pk_fp8_f32 v38, v44, v45 op_sel:[0,0,1]
	v_cvt_pk_fp8_f32 v39, v36, v37 op_sel:[0,0,1]
	ds_write_b64 v122, v[38:39] offset:768
	v_add_u32_e32 v38, 0x80, v106
	ds_read_b128 v[34:37], v108
	v_ashrrev_i32_e32 v39, 31, v38
	v_lshlrev_b64 v[38:39], 10, v[38:39]
	v_lshl_add_u64 v[38:39], s[16:17], 0, v[38:39]
	v_lshl_add_u64 v[38:39], v[38:39], 0, s[8:9]
	v_lshl_add_u64 v[38:39], v[38:39], 0, v[142:143]
	s_waitcnt lgkmcnt(0)
	global_store_dwordx4 v[38:39], v[34:37], off
	s_nop 1
	v_mul_f32_e32 v34, 0x3d800000, v171
	v_pk_fma_f32 v[26:27], v[34:35], v[26:27], v[150:151] op_sel_hi:[0,1,1]
	v_med3_f32 v26, v26, s73, v184
	v_med3_f32 v27, v27, s73, v184
	v_exp_f32_e64 v36, -v26
	v_exp_f32_e64 v37, -v27
	v_pk_fma_f32 v[28:29], v[34:35], v[28:29], v[156:157] op_sel_hi:[0,1,1]
	v_pk_fma_f32 v[30:31], v[34:35], v[30:31], v[152:153] op_sel_hi:[0,1,1]
	v_pk_fma_f32 v[32:33], v[34:35], v[32:33], v[154:155] op_sel_hi:[0,1,1]
	v_pk_add_f32 v[36:37], v[36:37], 1.0 op_sel_hi:[1,0]
	v_med3_f32 v30, v30, s70, v167
	v_med3_f32 v31, v31, s70, v167
	v_med3_f32 v28, v28, s73, v184
	v_med3_f32 v29, v29, s73, v184
	v_pk_fma_f32 v[18:19], v[34:35], v[18:19], v[86:87] op_sel_hi:[0,1,1]
	v_pk_mul_f32 v[26:27], v[26:27], v[30:31]
	v_med3_f32 v30, v32, s70, v167
	v_med3_f32 v31, v33, s70, v167
	v_exp_f32_e64 v32, -v28
	v_exp_f32_e64 v33, -v29
	v_med3_f32 v18, v18, s73, v184
	v_med3_f32 v19, v19, s73, v184
	v_pk_fma_f32 v[20:21], v[34:35], v[20:21], v[88:89] op_sel_hi:[0,1,1]
	v_pk_add_f32 v[32:33], v[32:33], 1.0 op_sel_hi:[1,0]
	v_pk_fma_f32 v[22:23], v[34:35], v[22:23], v[82:83] op_sel_hi:[0,1,1]
	v_pk_mul_f32 v[180:181], v[36:37], v[32:33]
	v_rcp_f32_e32 v180, v180
	v_rcp_f32_e32 v181, v181
	s_nop 0
	v_pk_mul_f32 v[182:183], v[180:181], v[32:33]
	v_pk_mul_f32 v[32:33], v[180:181], v[36:37]
	v_pk_mul_f32 v[26:27], v[26:27], v[182:183]
	v_pk_fma_f32 v[24:25], v[34:35], v[24:25], v[84:85] op_sel_hi:[0,1,1]
	v_med3_f32 v22, v22, s70, v167
	v_med3_f32 v23, v23, s70, v167
	v_pk_mul_f32 v[28:29], v[28:29], v[32:33]
	v_med3_f32 v20, v20, s73, v184
	v_pk_mul_f32 v[28:29], v[28:29], v[30:31]
	v_exp_f32_e64 v30, -v18
	v_exp_f32_e64 v31, -v19
	v_med3_f32 v21, v21, s73, v184
	v_pk_add_f32 v[30:31], v[30:31], 1.0 op_sel_hi:[1,0]
	s_nop 0
	s_nop 0
	s_nop 0
	v_pk_mul_f32 v[18:19], v[18:19], v[22:23]
	v_med3_f32 v22, v24, s70, v167
	v_med3_f32 v23, v25, s70, v167
	v_exp_f32_e64 v24, -v20
	v_exp_f32_e64 v25, -v21
	s_nop 0
	v_pk_add_f32 v[24:25], v[24:25], 1.0 op_sel_hi:[1,0]
	s_nop 0
	v_pk_mul_f32 v[180:181], v[30:31], v[24:25]
	v_rcp_f32_e32 v180, v180
	v_rcp_f32_e32 v181, v181
	s_nop 0
	v_pk_mul_f32 v[182:183], v[180:181], v[24:25]
	v_pk_mul_f32 v[24:25], v[180:181], v[30:31]
	v_pk_mul_f32 v[18:19], v[18:19], v[182:183]
	s_nop 0
	v_pk_mul_f32 v[20:21], v[20:21], v[24:25]
	s_nop 0
	v_pk_mul_f32 v[20:21], v[20:21], v[22:23]
	v_mov_b32_e32 v23, v143
	v_cvt_pk_fp8_f32 v23, v18, v19
	v_mul_f32_e32 v18, 0x3d800000, v168
	v_pk_fma_f32 v[10:11], v[18:19], v[10:11], v[150:151] op_sel_hi:[0,1,1]
	v_med3_f32 v10, v10, s73, v184
	v_med3_f32 v11, v11, s73, v184
	v_cvt_pk_fp8_f32 v23, v20, v21 op_sel:[0,0,1]
	v_exp_f32_e64 v20, -v10
	v_exp_f32_e64 v21, -v11
	v_pk_fma_f32 v[12:13], v[18:19], v[12:13], v[156:157] op_sel_hi:[0,1,1]
	v_pk_fma_f32 v[14:15], v[18:19], v[14:15], v[152:153] op_sel_hi:[0,1,1]
	v_pk_fma_f32 v[16:17], v[18:19], v[16:17], v[154:155] op_sel_hi:[0,1,1]
	v_pk_add_f32 v[20:21], v[20:21], 1.0 op_sel_hi:[1,0]
	v_med3_f32 v14, v14, s70, v167
	v_med3_f32 v15, v15, s70, v167
	v_med3_f32 v12, v12, s73, v184
	v_med3_f32 v13, v13, s73, v184
	v_pk_fma_f32 v[2:3], v[18:19], v[2:3], v[86:87] op_sel_hi:[0,1,1]
	v_pk_mul_f32 v[10:11], v[10:11], v[14:15]
	v_med3_f32 v14, v16, s70, v167
	v_med3_f32 v15, v17, s70, v167
	v_exp_f32_e64 v16, -v12
	v_exp_f32_e64 v17, -v13
	v_med3_f32 v2, v2, s73, v184
	v_med3_f32 v3, v3, s73, v184
	v_pk_fma_f32 v[4:5], v[18:19], v[4:5], v[88:89] op_sel_hi:[0,1,1]
	v_pk_add_f32 v[16:17], v[16:17], 1.0 op_sel_hi:[1,0]
	v_pk_fma_f32 v[6:7], v[18:19], v[6:7], v[82:83] op_sel_hi:[0,1,1]
	v_pk_mul_f32 v[180:181], v[20:21], v[16:17]
	v_rcp_f32_e32 v180, v180
	v_rcp_f32_e32 v181, v181
	s_nop 0
	v_pk_mul_f32 v[182:183], v[180:181], v[16:17]
	v_pk_mul_f32 v[16:17], v[180:181], v[20:21]
	v_pk_mul_f32 v[10:11], v[10:11], v[182:183]
	v_pk_fma_f32 v[8:9], v[18:19], v[8:9], v[84:85] op_sel_hi:[0,1,1]
	v_med3_f32 v6, v6, s70, v167
	v_med3_f32 v7, v7, s70, v167
	v_pk_mul_f32 v[12:13], v[12:13], v[16:17]
	v_med3_f32 v4, v4, s73, v184
	v_pk_mul_f32 v[12:13], v[12:13], v[14:15]
	v_exp_f32_e64 v14, -v2
	v_exp_f32_e64 v15, -v3
	v_med3_f32 v5, v5, s73, v184
	v_mov_b32_e32 v22, v143
	v_cvt_pk_fp8_f32 v22, v26, v27
	v_pk_add_f32 v[14:15], v[14:15], 1.0 op_sel_hi:[1,0]
	v_cvt_pk_fp8_f32 v22, v28, v29 op_sel:[0,0,1]
	ds_write_b64 v122, v[22:23]
	s_nop 0
	v_pk_mul_f32 v[2:3], v[2:3], v[6:7]
	v_med3_f32 v6, v8, s70, v167
	v_med3_f32 v7, v9, s70, v167
	v_exp_f32_e64 v8, -v4
	v_exp_f32_e64 v9, -v5
	s_nop 0
	v_pk_add_f32 v[8:9], v[8:9], 1.0 op_sel_hi:[1,0]
	s_nop 0
	v_pk_mul_f32 v[180:181], v[14:15], v[8:9]
	v_rcp_f32_e32 v180, v180
	v_rcp_f32_e32 v181, v181
	s_nop 0
	v_pk_mul_f32 v[182:183], v[180:181], v[8:9]
	v_pk_mul_f32 v[8:9], v[180:181], v[14:15]
	v_pk_mul_f32 v[2:3], v[2:3], v[182:183]
	s_nop 0
	v_pk_mul_f32 v[4:5], v[4:5], v[8:9]
	s_nop 0
	v_pk_mul_f32 v[4:5], v[4:5], v[6:7]
	v_mov_b32_e32 v6, v143
	v_mov_b32_e32 v7, v143
	v_cvt_pk_fp8_f32 v6, v10, v11
	v_cvt_pk_fp8_f32 v7, v2, v3
	v_cvt_pk_fp8_f32 v6, v12, v13 op_sel:[0,0,1]
	v_cvt_pk_fp8_f32 v7, v4, v5 op_sel:[0,0,1]
	ds_write_b64 v122, v[6:7] offset:768
	v_add_u32_e32 v6, 0xa0, v106
	ds_read_b128 v[2:5], v108
	v_ashrrev_i32_e32 v7, 31, v6
	v_lshlrev_b64 v[6:7], 10, v[6:7]
	v_lshl_add_u64 v[6:7], s[16:17], 0, v[6:7]
	v_lshl_add_u64 v[6:7], v[6:7], 0, s[8:9]
	v_lshl_add_u64 v[6:7], v[6:7], 0, v[142:143]
	s_mov_b64 s[8:9], -1
	s_waitcnt lgkmcnt(0)
	global_store_dwordx4 v[6:7], v[2:5], off
	s_cbranch_vccnz .LBB0_1537
	s_lshl_b64 s[6:7], s[74:75], 12
	s_add_u32 s9, s33, s6
	s_addc_u32 s69, s54, s7
	s_lshl_b32 s6, s68, 7
	s_ashr_i32 s7, s6, 31
	v_mov_b32_e32 v2, v0
	s_lshl_b64 s[6:7], s[6:7], 1
	s_add_u32 s6, s9, s6
	v_readfirstlane_b32 s8, v2
	s_addc_u32 s7, s69, s7
	s_and_b32 s9, s8, 0xc0
	s_add_u32 s6, s6, s9
	s_addc_u32 s7, s7, 0
	v_and_b32_e32 v3, 48, v2
	global_load_dwordx4 v[86:89], v3, s[6:7]
	global_load_dwordx4 v[82:85], v3, s[6:7] offset:2048
	s_ashr_i32 s7, s8, 2
	s_lshl_b32 s6, s72, 8
	s_andn2_b32 s7, s7, 63
	s_add_i32 s7, s7, s6
	v_and_or_b32 v2, v2, 15, s7
	v_ashrrev_i32_e32 v3, 31, v2
	v_lshl_add_u64 v[4:5], v[2:3], 2, s[12:13]
	v_add_u32_e32 v6, 0x80, v2
	v_add_u32_e32 v8, 0x90, v2
	v_add_u32_e32 v10, 0xa0, v2
	v_add_u32_e32 v2, 0xb0, v2
	v_ashrrev_i32_e32 v7, 31, v6
	v_ashrrev_i32_e32 v9, 31, v8
	v_ashrrev_i32_e32 v11, 31, v10
	v_ashrrev_i32_e32 v3, 31, v2
	v_lshl_add_u64 v[6:7], v[6:7], 2, s[12:13]
	v_lshl_add_u64 v[8:9], v[8:9], 2, s[12:13]
	v_lshl_add_u64 v[10:11], v[10:11], 2, s[12:13]
	v_lshl_add_u64 v[2:3], v[2:3], 2, s[12:13]
	global_load_dword v177, v[4:5], off
	global_load_dword v176, v[4:5], off offset:64
	global_load_dword v175, v[4:5], off offset:128
	global_load_dword v174, v[4:5], off offset:192
	global_load_dword v173, v[6:7], off
	global_load_dword v172, v[8:9], off
	global_load_dword v171, v[10:11], off
	global_load_dword v168, v[2:3], off
	s_andn2_b64 vcc, exec, s[14:15]
	s_cbranch_vccnz .LBB0_1536
	s_barrier
	s_branch .LBB0_1536
